# hoisted four-waves-per-row scanner that publishes a row's raw list two pieces into the next row, so the row transition no longer waits for the LDS writes
# baseline (speedup 1.0000x reference)
.Lsc_s1:
	s_add_u32 s40, s39, 0x400
	buffer_load_dwordx4 v[104:107], v6, s[28:31], s40 offen nt
	s_cmp_eq_u32 s35, 0
	s_cbranch_scc1 .Lsc_nopub
	s_waitcnt lgkmcnt(0)
	v_mov_b32_e32 v12, s56
	ds_write_b32 v28, v12
.Lsc_nopub:
	s_waitcnt vmcnt(9)
	v_or3_b32 v12, v108, v109, v110
	v_bitop3_b32 v12, v12, s9, v111 bitop3:0xc8
	v_cmp_ne_u32_e32 vcc, 0, v12
	s_cbranch_vccz .Lsc_s2
	s_bcnt1_i32_b64 s40, vcc
	v_mbcnt_lo_u32_b32 v13, vcc_lo, 0
	v_mbcnt_hi_u32_b32 v13, vcc_hi, v13
	v_add_u32_e32 v13, s42, v13
	s_add_i32 s42, s42, s40
	v_cmp_gt_i32_e64 s[0:1], s7, v13
	s_and_b64 s[4:5], vcc, s[0:1]
	s_and_saveexec_b64 s[0:1], s[4:5]
	v_lshl_add_u32 v14, v13, 4, v9
	v_lshl_add_u32 v15, v13, 2, v10
	v_add_u32_e32 v13, 0x200, v8
	ds_write_b128 v14, v[108:111]
	ds_write_b32 v15, v13
	s_mov_b64 exec, -1

.Lsc_s9:
	s_add_u32 s40, s39, 0x2400
	buffer_load_dwordx4 v[136:139], v7, s[28:31], s40 offen nt
	s_add_i32 s56, s42, 1
	v_mov_b32_e32 v28, v11
	s_cmp_eq_u32 s35, s36
	s_cbranch_scc0 .Lsc_adv
	s_waitcnt lgkmcnt(0)
	v_mov_b32_e32 v12, s56
	ds_write_b32 v28, v12
	s_branch .LBB1_384
.Lsc_adv:
	s_add_i32 s35, s35, 1
	s_mov_b32 s38, s39
	s_branch .Lsc_row
